# GEMM K-loops of phases 1,5,6,7,11: per-lane LDS/DMA offset constants computed on the first K-trip of a unit only instead of every trip (they are trip-invariant); stacks on unscaled fp8 MFMA + NSA mask
# speedup vs baseline: 1.0449x; 1.0122x over previous
.LBB0_982:
	s_cmpk_lg_i32 s97, 0x180
	s_cbranch_scc1 .Lp1_fast
	v_add_u32_e32 v129, s31, v128
	v_ashrrev_i32_e32 v131, 3, v129
	v_lshlrev_b32_e32 v130, 4, v128
	v_lshlrev_b32_e32 v136, 1, v131
	v_lshrrev_b32_e32 v137, 2, v131
	v_bitop3_b32 v130, v129, s55, v130 bitop3:0x48
	v_and_b32_e32 v136, 24, v136
	v_and_b32_e32 v137, 4, v137
	v_and_b32_e32 v138, 0x1fffe3, v131
	v_lshl_add_u32 v129, v129, 4, v132
	v_or3_b32 v136, v138, v137, v136
	v_ashrrev_i32_e32 v129, 7, v129
	v_lshl_or_b32 v244, v136, 11, v130
	v_lshlrev_b32_e32 v136, 1, v129
	v_lshrrev_b32_e32 v137, 2, v129
	v_and_b32_e32 v136, 24, v136
	v_and_b32_e32 v137, 4, v137
	v_and_b32_e32 v138, 0x1fffe3, v129
	v_or3_b32 v136, v138, v137, v136
	v_lshl_or_b32 v245, v136, 11, v130
	v_and_b32_e32 v136, 15, v128
	v_lshrrev_b32_e32 v137, 3, v128
	v_bfe_u32 v128, v128, 1, 3
	s_mov_b32 s10, 0xffffffe
	v_lshlrev_b32_e32 v136, 7, v136
	v_and_b32_e32 v138, 0xffffffe, v137
	v_bitop3_b32 v137, v137, v128, s10 bitop3:0x6c
	v_or_b32_e32 v168, s70, v136
	v_or_b32_e32 v136, s71, v136
	v_lshlrev_b32_e32 v169, 4, v137
	v_bitop3_b32 v128, v138, v128, 1 bitop3:0x36
	v_add_u32_e32 v246, v169, v136
	v_lshlrev_b32_e32 v128, 4, v128
	v_add_u32_e32 v247, v128, v136
	v_lshl_or_b32 v249, v129, 11, v130
	v_add_u32_e32 v129, s85, v246
	v_lshl_or_b32 v248, v131, 11, v130
	v_add_u32_e32 v130, s85, v247
	v_add_u32_e32 v250, 0x40000, v248
	v_add_u32_e32 v251, 0x40000, v249
	v_add3_u32 v252, v169, v168, 0
	v_add3_u32 v253, v128, v168, 0
	s_branch .Lp1_join
.Lp1_fast:
	v_add_u32_e32 v129, s85, v246
	v_add_u32_e32 v130, s85, v247
.Lp1_join:
	ds_read_b128 v[136:139], v129
	ds_read_b128 v[144:147], v129 offset:2048
	ds_read_b128 v[140:143], v130
	ds_read_b128 v[148:151], v130 offset:2048
	v_add_u32_e32 v129, s86, v246
	v_add_u32_e32 v130, s86, v247
	ds_read_b128 v[152:155], v129
	ds_read_b128 v[160:163], v129 offset:2048
	ds_read_b128 v[156:159], v130
	ds_read_b128 v[164:167], v130 offset:2048
	s_add_i32 s10, s97, 0xffffff80
	s_add_i32 s11, s10, s94
	s_cmpk_eq_i32 s97, 0x880
	s_cselect_b32 s40, s37, s91
	s_cselect_b32 s10, 0, s10
	s_cselect_b32 s39, 0x80, s97
	s_cselect_b32 s38, s36, s11
	s_add_i32 s11, s91, s97
	s_add_i32 s39, s40, s39
	s_addk_i32 s11, 0xff00
	s_add_i32 s40, s40, s10
	s_mov_b32 m0, s72
	ds_read_b128 v[168:171], v252
	ds_read_b128 v[176:179], v252 offset:2048
	ds_read_b128 v[172:175], v253
	ds_read_b128 v[180:183], v253 offset:2048
	ds_read_b128 v[184:187], v252 offset:4096
	ds_read_b128 v[192:195], v252 offset:6144
	ds_read_b128 v[188:191], v253 offset:4096
	ds_read_b128 v[196:199], v253 offset:6144
	buffer_load_dwordx4 v250, s[12:15], s11 offen lds
	s_mov_b32 m0, s75
	s_nop 0
	buffer_load_dwordx4 v251, s[12:15], s11 offen lds
	s_waitcnt vmcnt(8)
	s_waitcnt lgkmcnt(0)
	s_barrier
	s_setprio 1
	s_waitcnt lgkmcnt(5)
	v_mfma_f32_16x16x128_f8f6f4 v[124:127], v[136:143], v[168:175], v[124:127]
	v_mfma_f32_16x16x128_f8f6f4 v[120:123], v[144:151], v[168:175], v[120:123]
	s_waitcnt lgkmcnt(4)
	v_mfma_f32_16x16x128_f8f6f4 v[112:115], v[136:143], v[176:183], v[112:115]
	v_mfma_f32_16x16x128_f8f6f4 v[104:107], v[144:151], v[176:183], v[104:107]
	s_waitcnt lgkmcnt(1)
	v_mfma_f32_16x16x128_f8f6f4 v[96:99], v[136:143], v[184:191], v[96:99]
	v_mfma_f32_16x16x128_f8f6f4 v[128:131], v[144:151], v[184:191], v[88:91]
	s_waitcnt lgkmcnt(0)
	v_mfma_f32_16x16x128_f8f6f4 v[200:203], v[136:143], v[192:199], v[80:83]
	v_mfma_f32_16x16x128_f8f6f4 v[204:207], v[144:151], v[192:199], v[72:75]
	s_setprio 0
	s_setprio 1
	v_mfma_f32_16x16x128_f8f6f4 v[116:119], v[152:159], v[168:175], v[116:119]
	v_mfma_f32_16x16x128_f8f6f4 v[108:111], v[160:167], v[168:175], v[108:111]
	v_mfma_f32_16x16x128_f8f6f4 v[100:103], v[152:159], v[176:183], v[100:103]
	v_mfma_f32_16x16x128_f8f6f4 v[168:171], v[160:167], v[176:183], v[92:95]
	v_mfma_f32_16x16x128_f8f6f4 v[172:175], v[152:159], v[184:191], v[84:87]
	v_mfma_f32_16x16x128_f8f6f4 v[176:179], v[160:167], v[184:191], v[76:79]
	v_mfma_f32_16x16x128_f8f6f4 v[180:183], v[152:159], v[192:199], v[68:71]
	v_mfma_f32_16x16x128_f8f6f4 v[184:187], v[160:167], v[192:199], v[64:67]
	s_setprio 0
	s_barrier
	s_mov_b32 m0, s57
	s_mov_b32 s10, s14
	s_mov_b32 s11, s15
	s_nop 1
	ds_read_b128 v[64:67], v252 offset:16384
	ds_read_b128 v[72:75], v252 offset:18432
	ds_read_b128 v[68:71], v253 offset:16384
	ds_read_b128 v[76:79], v253 offset:18432
	ds_read_b128 v[80:83], v252 offset:20480
	ds_read_b128 v[88:91], v252 offset:22528
	ds_read_b128 v[84:87], v253 offset:20480
	ds_read_b128 v[92:95], v253 offset:22528
	buffer_load_dwordx4 v244, s[8:11], s38 offen lds
	s_mov_b32 m0, s58
	s_add_i32 s41, s38, 0x40000
	buffer_load_dwordx4 v245, s[8:11], s38 offen lds
	s_mov_b32 m0, s59
	s_nop 0
	buffer_load_dwordx4 v244, s[8:11], s41 offen lds
	s_mov_b32 m0, s60
	s_nop 0
	buffer_load_dwordx4 v245, s[8:11], s41 offen lds
	s_mov_b32 m0, s56
	s_nop 0
	buffer_load_dwordx4 v248, s[12:15], s40 offen lds
	s_mov_b32 m0, s61
	s_nop 0
	buffer_load_dwordx4 v249, s[12:15], s40 offen lds
	s_waitcnt vmcnt(8)
	s_waitcnt lgkmcnt(0)
	s_barrier
	s_setprio 1
	s_waitcnt lgkmcnt(5)
	v_mfma_f32_16x16x128_f8f6f4 v[60:63], v[136:143], v[64:71], v[60:63]
	v_mfma_f32_16x16x128_f8f6f4 v[56:59], v[144:151], v[64:71], v[56:59]
	s_waitcnt lgkmcnt(4)
	v_mfma_f32_16x16x128_f8f6f4 v[48:51], v[136:143], v[72:79], v[48:51]
	v_mfma_f32_16x16x128_f8f6f4 v[188:191], v[144:151], v[72:79], v[40:43]
	s_waitcnt lgkmcnt(1)
	v_mfma_f32_16x16x128_f8f6f4 v[192:195], v[136:143], v[80:87], v[32:35]
	v_mfma_f32_16x16x128_f8f6f4 v[196:199], v[144:151], v[80:87], v[24:27]
	s_waitcnt lgkmcnt(0)
	v_mfma_f32_16x16x128_f8f6f4 v[208:211], v[136:143], v[88:95], v[16:19]
	v_mfma_f32_16x16x128_f8f6f4 v[212:215], v[144:151], v[88:95], v[8:11]
	s_setprio 0
	s_setprio 1
	v_mfma_f32_16x16x128_f8f6f4 v[52:55], v[152:159], v[64:71], v[52:55]
	v_mfma_f32_16x16x128_f8f6f4 v[216:219], v[160:167], v[64:71], v[44:47]
	v_mfma_f32_16x16x128_f8f6f4 v[220:223], v[152:159], v[72:79], v[36:39]
	v_mfma_f32_16x16x128_f8f6f4 v[224:227], v[160:167], v[72:79], v[28:31]
	v_mfma_f32_16x16x128_f8f6f4 v[228:231], v[152:159], v[80:87], v[20:23]
	v_mfma_f32_16x16x128_f8f6f4 v[232:235], v[160:167], v[80:87], v[12:15]
	v_mfma_f32_16x16x128_f8f6f4 v[236:239], v[152:159], v[88:95], v[4:7]
	v_mfma_f32_16x16x128_f8f6f4 v[240:243], v[160:167], v[88:95], v[0:3]
	s_setprio 0
	s_barrier
	s_add_i32 s41, 0, 0x18000
	s_nop 2
	v_add_u32_e32 v4, s41, v246
	v_add_u32_e32 v12, s41, v247
	s_add_i32 s41, 0, 0x1c000
	v_add_u32_e32 v16, s41, v246
	ds_read_b128 v[0:3], v4
	ds_read_b128 v[8:11], v4 offset:2048
	ds_read_b128 v[4:7], v12
	ds_read_b128 v[12:15], v12 offset:2048
	v_add_u32_e32 v17, s41, v247
	ds_read_b128 v[136:139], v16
	ds_read_b128 v[144:147], v16 offset:2048
	ds_read_b128 v[140:143], v17
	ds_read_b128 v[148:151], v17 offset:2048
	s_mov_b32 m0, s62
	ds_read_b128 v[16:19], v252 offset:32768
	ds_read_b128 v[24:27], v252 offset:34816
	ds_read_b128 v[20:23], v253 offset:32768
	ds_read_b128 v[28:31], v253 offset:34816
	ds_read_b128 v[32:35], v252 offset:36864
	ds_read_b128 v[40:43], v252 offset:38912
	ds_read_b128 v[36:39], v253 offset:36864
	ds_read_b128 v[44:47], v253 offset:38912
	buffer_load_dwordx4 v250, s[12:15], s40 offen lds
	s_mov_b32 m0, s63
	s_nop 0
	buffer_load_dwordx4 v251, s[12:15], s40 offen lds
	s_waitcnt vmcnt(8)
	s_waitcnt lgkmcnt(0)
	s_barrier
	s_setprio 1
	s_waitcnt lgkmcnt(5)
	v_mfma_f32_16x16x128_f8f6f4 v[124:127], v[0:7], v[16:23], v[124:127]
	v_mfma_f32_16x16x128_f8f6f4 v[120:123], v[8:15], v[16:23], v[120:123]
	s_waitcnt lgkmcnt(4)
	v_mfma_f32_16x16x128_f8f6f4 v[112:115], v[0:7], v[24:31], v[112:115]
	v_mfma_f32_16x16x128_f8f6f4 v[104:107], v[8:15], v[24:31], v[104:107]
	s_waitcnt lgkmcnt(1)
	v_mfma_f32_16x16x128_f8f6f4 v[96:99], v[0:7], v[32:39], v[96:99]
	v_mfma_f32_16x16x128_f8f6f4 v[88:91], v[8:15], v[32:39], v[128:131]
	s_waitcnt lgkmcnt(0)
	v_mfma_f32_16x16x128_f8f6f4 v[80:83], v[0:7], v[40:47], v[200:203]
	v_mfma_f32_16x16x128_f8f6f4 v[72:75], v[8:15], v[40:47], v[204:207]
	s_setprio 0
	s_setprio 1
	v_mfma_f32_16x16x128_f8f6f4 v[116:119], v[136:143], v[16:23], v[116:119]
	v_mfma_f32_16x16x128_f8f6f4 v[108:111], v[144:151], v[16:23], v[108:111]
	v_mfma_f32_16x16x128_f8f6f4 v[100:103], v[136:143], v[24:31], v[100:103]
	v_mfma_f32_16x16x128_f8f6f4 v[92:95], v[144:151], v[24:31], v[168:171]
	v_mfma_f32_16x16x128_f8f6f4 v[84:87], v[136:143], v[32:39], v[172:175]
	v_mfma_f32_16x16x128_f8f6f4 v[76:79], v[144:151], v[32:39], v[176:179]
	v_mfma_f32_16x16x128_f8f6f4 v[68:71], v[136:143], v[40:47], v[180:183]
	v_mfma_f32_16x16x128_f8f6f4 v[64:67], v[144:151], v[40:47], v[184:187]
	s_setprio 0
	s_barrier
	s_mov_b32 m0, s64
	s_add_i32 s40, s38, 0x80
	ds_read_b128 v[152:155], v252 offset:49152
	ds_read_b128 v[160:163], v252 offset:51200
	ds_read_b128 v[156:159], v253 offset:49152
	ds_read_b128 v[164:167], v253 offset:51200
	ds_read_b128 v[168:171], v252 offset:53248
	ds_read_b128 v[176:179], v252 offset:55296
	ds_read_b128 v[172:175], v253 offset:53248
	ds_read_b128 v[180:183], v253 offset:55296
	buffer_load_dwordx4 v244, s[8:11], s40 offen lds
	s_mov_b32 m0, s65
	s_add_i32 s38, s38, 0x40080
	buffer_load_dwordx4 v245, s[8:11], s40 offen lds
	s_mov_b32 m0, s68
	s_nop 0
	buffer_load_dwordx4 v244, s[8:11], s38 offen lds
	s_mov_b32 m0, s69
	s_nop 0
	buffer_load_dwordx4 v245, s[8:11], s38 offen lds
	s_mov_b32 m0, s66
	s_nop 0
	buffer_load_dwordx4 v248, s[12:15], s39 offen lds
	s_mov_b32 m0, s67
	s_nop 0
	buffer_load_dwordx4 v249, s[12:15], s39 offen lds
	s_waitcnt vmcnt(8)
	s_waitcnt lgkmcnt(0)
	s_barrier
	s_setprio 1
	s_waitcnt lgkmcnt(5)
	v_mfma_f32_16x16x128_f8f6f4 v[60:63], v[0:7], v[152:159], v[60:63]
	v_mfma_f32_16x16x128_f8f6f4 v[56:59], v[8:15], v[152:159], v[56:59]
	s_waitcnt lgkmcnt(4)
	v_mfma_f32_16x16x128_f8f6f4 v[48:51], v[0:7], v[160:167], v[48:51]
	v_mfma_f32_16x16x128_f8f6f4 v[40:43], v[8:15], v[160:167], v[188:191]
	s_waitcnt lgkmcnt(1)
	v_mfma_f32_16x16x128_f8f6f4 v[32:35], v[0:7], v[168:175], v[192:195]
	v_mfma_f32_16x16x128_f8f6f4 v[24:27], v[8:15], v[168:175], v[196:199]
	s_waitcnt lgkmcnt(0)
	v_mfma_f32_16x16x128_f8f6f4 v[16:19], v[0:7], v[176:183], v[208:211]
	v_mfma_f32_16x16x128_f8f6f4 v[8:11], v[8:15], v[176:183], v[212:215]
	s_setprio 0
	s_setprio 1
	v_mfma_f32_16x16x128_f8f6f4 v[52:55], v[136:143], v[152:159], v[52:55]
	v_mfma_f32_16x16x128_f8f6f4 v[44:47], v[144:151], v[152:159], v[216:219]
	v_mfma_f32_16x16x128_f8f6f4 v[36:39], v[136:143], v[160:167], v[220:223]
	v_mfma_f32_16x16x128_f8f6f4 v[28:31], v[144:151], v[160:167], v[224:227]
	v_mfma_f32_16x16x128_f8f6f4 v[20:23], v[136:143], v[168:175], v[228:231]
	v_mfma_f32_16x16x128_f8f6f4 v[12:15], v[144:151], v[168:175], v[232:235]
	v_mfma_f32_16x16x128_f8f6f4 v[4:7], v[136:143], v[176:183], v[236:239]
	v_mfma_f32_16x16x128_f8f6f4 v[0:3], v[144:151], v[176:183], v[240:243]
	s_setprio 0
	s_barrier
	s_add_i32 s96, s96, 2
	s_addk_i32 s97, 0x100
	s_cmp_gt_u32 s96, 13
	s_cbranch_scc1 .LBB0_1022

.LBB0_2173:
	s_cmpk_lg_i32 s62, 0x180
	s_cbranch_scc1 .Lp5_fast
	v_add_u32_e32 v129, s17, v128
	v_lshlrev_b32_e32 v130, 4, v128
	v_ashrrev_i32_e32 v131, 3, v129
	v_bitop3_b32 v130, v129, s22, v130 bitop3:0x48
	v_lshlrev_b32_e32 v132, 1, v131
	v_lshrrev_b32_e32 v133, 2, v131
	v_lshl_add_u32 v129, v129, 4, v134
	v_and_b32_e32 v132, 24, v132
	v_and_b32_e32 v133, 4, v133
	v_and_b32_e32 v136, 0x1fffe3, v131
	v_ashrrev_i32_e32 v129, 7, v129
	v_or3_b32 v132, v136, v133, v132
	v_lshlrev_b32_e32 v133, 1, v129
	v_lshrrev_b32_e32 v136, 2, v129
	v_and_b32_e32 v133, 24, v133
	v_and_b32_e32 v136, 4, v136
	v_and_b32_e32 v137, 0x1fffe3, v129
	v_or3_b32 v133, v137, v136, v133
	v_and_b32_e32 v136, 15, v128
	v_lshrrev_b32_e32 v137, 3, v128
	v_bfe_u32 v128, v128, 1, 3
	v_lshlrev_b32_e32 v136, 7, v136
	v_and_b32_e32 v138, 0xffffffe, v137
	v_bitop3_b32 v137, v137, v128, s48 bitop3:0x6c
	v_or_b32_e32 v168, s42, v136
	v_or_b32_e32 v136, s43, v136
	v_lshlrev_b32_e32 v169, 4, v137
	v_bitop3_b32 v128, v138, v128, 1 bitop3:0x36
	v_add_u32_e32 v244, v169, v136
	v_lshlrev_b32_e32 v128, 4, v128
	v_add_u32_e32 v245, v128, v136
	v_lshl_or_b32 v247, v129, 11, v130
	v_add_u32_e32 v129, s49, v244
	v_lshl_or_b32 v132, v132, 11, v130
	v_lshl_or_b32 v133, v133, 11, v130
	v_lshl_or_b32 v246, v131, 11, v130
	v_add_u32_e32 v130, s49, v245
	v_add_u32_e32 v248, 0x40000, v246
	v_add_u32_e32 v249, 0x40000, v247
	v_add3_u32 v250, v169, v168, 0
	v_add3_u32 v251, v128, v168, 0
	s_branch .Lp5_join
.Lp5_fast:
	v_add_u32_e32 v129, s49, v244
	v_add_u32_e32 v130, s49, v245
.Lp5_join:
	ds_read_b128 v[136:139], v129
	ds_read_b128 v[144:147], v129 offset:2048
	ds_read_b128 v[140:143], v130
	ds_read_b128 v[148:151], v130 offset:2048
	v_add_u32_e32 v129, s50, v244
	v_add_u32_e32 v130, s50, v245
	ds_read_b128 v[152:155], v129
	ds_read_b128 v[160:163], v129 offset:2048
	ds_read_b128 v[156:159], v130
	ds_read_b128 v[164:167], v130 offset:2048
	s_add_i32 s6, s62, 0xffffff80
	s_add_i32 s7, s6, s57
	s_cmpk_eq_i32 s62, 0x880
	s_cselect_b32 s65, s35, s54
	s_cselect_b32 s6, 0, s6
	s_cselect_b32 s64, 0x80, s62
	s_cselect_b32 s63, s29, s7
	s_add_i32 s7, s54, s62
	s_add_i32 s64, s65, s64
	s_addk_i32 s7, 0xff00
	s_add_i32 s65, s65, s6
	s_mov_b32 m0, s44
	ds_read_b128 v[168:171], v250
	ds_read_b128 v[176:179], v250 offset:2048
	ds_read_b128 v[172:175], v251
	ds_read_b128 v[180:183], v251 offset:2048
	ds_read_b128 v[184:187], v250 offset:4096
	ds_read_b128 v[192:195], v250 offset:6144
	ds_read_b128 v[188:191], v251 offset:4096
	ds_read_b128 v[196:199], v251 offset:6144
	buffer_load_dwordx4 v248, s[8:11], s7 offen lds
	s_mov_b32 m0, s47
	s_nop 0
	buffer_load_dwordx4 v249, s[8:11], s7 offen lds
	s_waitcnt vmcnt(8)
	s_waitcnt lgkmcnt(0)
	s_barrier
	s_setprio 1
	s_waitcnt lgkmcnt(5)
	v_mfma_f32_16x16x128_f8f6f4 v[124:127], v[136:143], v[168:175], v[124:127]
	v_mfma_f32_16x16x128_f8f6f4 v[120:123], v[144:151], v[168:175], v[120:123]
	s_waitcnt lgkmcnt(4)
	v_mfma_f32_16x16x128_f8f6f4 v[108:111], v[136:143], v[176:183], v[108:111]
	v_mfma_f32_16x16x128_f8f6f4 v[104:107], v[144:151], v[176:183], v[104:107]
	s_waitcnt lgkmcnt(1)
	v_mfma_f32_16x16x128_f8f6f4 v[128:131], v[136:143], v[184:191], v[92:95]
	v_mfma_f32_16x16x128_f8f6f4 v[200:203], v[144:151], v[184:191], v[88:91]
	s_waitcnt lgkmcnt(0)
	v_mfma_f32_16x16x128_f8f6f4 v[204:207], v[136:143], v[192:199], v[76:79]
	v_mfma_f32_16x16x128_f8f6f4 v[208:211], v[144:151], v[192:199], v[72:75]
	s_setprio 0
	s_setprio 1
	v_mfma_f32_16x16x128_f8f6f4 v[116:119], v[152:159], v[168:175], v[116:119]
	v_mfma_f32_16x16x128_f8f6f4 v[112:115], v[160:167], v[168:175], v[112:115]
	v_mfma_f32_16x16x128_f8f6f4 v[100:103], v[152:159], v[176:183], v[100:103]
	v_mfma_f32_16x16x128_f8f6f4 v[96:99], v[160:167], v[176:183], v[96:99]
	v_mfma_f32_16x16x128_f8f6f4 v[168:171], v[152:159], v[184:191], v[84:87]
	v_mfma_f32_16x16x128_f8f6f4 v[172:175], v[160:167], v[184:191], v[80:83]
	v_mfma_f32_16x16x128_f8f6f4 v[176:179], v[152:159], v[192:199], v[68:71]
	v_mfma_f32_16x16x128_f8f6f4 v[180:183], v[160:167], v[192:199], v[64:67]
	s_setprio 0
	s_barrier
	s_mov_b32 m0, s26
	s_mov_b32 s6, s10
	s_mov_b32 s7, s11
	s_nop 1
	ds_read_b128 v[64:67], v250 offset:16384
	ds_read_b128 v[72:75], v250 offset:18432
	ds_read_b128 v[68:71], v251 offset:16384
	ds_read_b128 v[76:79], v251 offset:18432
	ds_read_b128 v[80:83], v250 offset:20480
	ds_read_b128 v[88:91], v250 offset:22528
	ds_read_b128 v[84:87], v251 offset:20480
	ds_read_b128 v[92:95], v251 offset:22528
	buffer_load_dwordx4 v132, s[4:7], s63 offen lds
	s_mov_b32 m0, s27
	s_add_i32 s66, s63, 0x40000
	buffer_load_dwordx4 v133, s[4:7], s63 offen lds
	s_mov_b32 m0, s28
	s_nop 0
	buffer_load_dwordx4 v132, s[4:7], s66 offen lds
	s_mov_b32 m0, s30
	s_nop 0
	buffer_load_dwordx4 v133, s[4:7], s66 offen lds
	s_mov_b32 m0, s25
	s_nop 0
	buffer_load_dwordx4 v246, s[8:11], s65 offen lds
	s_mov_b32 m0, s31
	s_nop 0
	buffer_load_dwordx4 v247, s[8:11], s65 offen lds
	s_waitcnt vmcnt(8)
	s_waitcnt lgkmcnt(0)
	s_barrier
	s_setprio 1
	s_waitcnt lgkmcnt(5)
	v_mfma_f32_16x16x128_f8f6f4 v[60:63], v[136:143], v[64:71], v[60:63]
	v_mfma_f32_16x16x128_f8f6f4 v[56:59], v[144:151], v[64:71], v[56:59]
	s_waitcnt lgkmcnt(4)
	v_mfma_f32_16x16x128_f8f6f4 v[184:187], v[136:143], v[72:79], v[44:47]
	v_mfma_f32_16x16x128_f8f6f4 v[188:191], v[144:151], v[72:79], v[40:43]
	s_waitcnt lgkmcnt(1)
	v_mfma_f32_16x16x128_f8f6f4 v[192:195], v[136:143], v[80:87], v[28:31]
	v_mfma_f32_16x16x128_f8f6f4 v[196:199], v[144:151], v[80:87], v[24:27]
	s_waitcnt lgkmcnt(0)
	v_mfma_f32_16x16x128_f8f6f4 v[212:215], v[136:143], v[88:95], v[12:15]
	v_mfma_f32_16x16x128_f8f6f4 v[216:219], v[144:151], v[88:95], v[8:11]
	s_setprio 0
	s_setprio 1
	v_mfma_f32_16x16x128_f8f6f4 v[52:55], v[152:159], v[64:71], v[52:55]
	v_mfma_f32_16x16x128_f8f6f4 v[48:51], v[160:167], v[64:71], v[48:51]
	v_mfma_f32_16x16x128_f8f6f4 v[220:223], v[152:159], v[72:79], v[36:39]
	v_mfma_f32_16x16x128_f8f6f4 v[224:227], v[160:167], v[72:79], v[32:35]
	v_mfma_f32_16x16x128_f8f6f4 v[228:231], v[152:159], v[80:87], v[20:23]
	v_mfma_f32_16x16x128_f8f6f4 v[232:235], v[160:167], v[80:87], v[16:19]
	v_mfma_f32_16x16x128_f8f6f4 v[236:239], v[152:159], v[88:95], v[4:7]
	v_mfma_f32_16x16x128_f8f6f4 v[240:243], v[160:167], v[88:95], v[0:3]
	s_setprio 0
	s_barrier
	s_add_i32 s66, 0, 0x18000
	s_nop 2
	v_add_u32_e32 v4, s66, v244
	v_add_u32_e32 v8, s66, v245
	s_add_i32 s66, 0, 0x1c000
	ds_read_b128 v[0:3], v4
	ds_read_b128 v[16:19], v4 offset:2048
	ds_read_b128 v[4:7], v8
	ds_read_b128 v[20:23], v8 offset:2048
	v_add_u32_e32 v8, s66, v244
	v_add_u32_e32 v9, s66, v245
	ds_read_b128 v[136:139], v8
	ds_read_b128 v[144:147], v8 offset:2048
	ds_read_b128 v[140:143], v9
	ds_read_b128 v[148:151], v9 offset:2048
	s_mov_b32 m0, s33
	ds_read_b128 v[8:11], v250 offset:32768
	ds_read_b128 v[24:27], v250 offset:34816
	ds_read_b128 v[12:15], v251 offset:32768
	ds_read_b128 v[28:31], v251 offset:34816
	ds_read_b128 v[32:35], v250 offset:36864
	ds_read_b128 v[40:43], v250 offset:38912
	ds_read_b128 v[36:39], v251 offset:36864
	ds_read_b128 v[44:47], v251 offset:38912
	buffer_load_dwordx4 v248, s[8:11], s65 offen lds
	s_mov_b32 m0, s34
	s_nop 0
	buffer_load_dwordx4 v249, s[8:11], s65 offen lds
	s_waitcnt vmcnt(8)
	s_waitcnt lgkmcnt(0)
	s_barrier
	s_setprio 1
	s_waitcnt lgkmcnt(5)
	v_mfma_f32_16x16x128_f8f6f4 v[124:127], v[0:7], v[8:15], v[124:127]
	v_mfma_f32_16x16x128_f8f6f4 v[120:123], v[16:23], v[8:15], v[120:123]
	s_waitcnt lgkmcnt(4)
	v_mfma_f32_16x16x128_f8f6f4 v[108:111], v[0:7], v[24:31], v[108:111]
	v_mfma_f32_16x16x128_f8f6f4 v[104:107], v[16:23], v[24:31], v[104:107]
	s_waitcnt lgkmcnt(1)
	v_mfma_f32_16x16x128_f8f6f4 v[92:95], v[0:7], v[32:39], v[128:131]
	v_mfma_f32_16x16x128_f8f6f4 v[88:91], v[16:23], v[32:39], v[200:203]
	s_waitcnt lgkmcnt(0)
	v_mfma_f32_16x16x128_f8f6f4 v[76:79], v[0:7], v[40:47], v[204:207]
	v_mfma_f32_16x16x128_f8f6f4 v[72:75], v[16:23], v[40:47], v[208:211]
	s_setprio 0
	s_setprio 1
	v_mfma_f32_16x16x128_f8f6f4 v[116:119], v[136:143], v[8:15], v[116:119]
	v_mfma_f32_16x16x128_f8f6f4 v[112:115], v[144:151], v[8:15], v[112:115]
	v_mfma_f32_16x16x128_f8f6f4 v[100:103], v[136:143], v[24:31], v[100:103]
	v_mfma_f32_16x16x128_f8f6f4 v[96:99], v[144:151], v[24:31], v[96:99]
	v_mfma_f32_16x16x128_f8f6f4 v[84:87], v[136:143], v[32:39], v[168:171]
	v_mfma_f32_16x16x128_f8f6f4 v[80:83], v[144:151], v[32:39], v[172:175]
	v_mfma_f32_16x16x128_f8f6f4 v[68:71], v[136:143], v[40:47], v[176:179]
	v_mfma_f32_16x16x128_f8f6f4 v[64:67], v[144:151], v[40:47], v[180:183]
	s_setprio 0
	s_barrier
	s_mov_b32 m0, s36
	s_add_i32 s65, s63, 0x80
	ds_read_b128 v[32:35], v250 offset:49152
	ds_read_b128 v[152:155], v250 offset:51200
	ds_read_b128 v[36:39], v251 offset:49152
	ds_read_b128 v[156:159], v251 offset:51200
	ds_read_b128 v[160:163], v250 offset:53248
	ds_read_b128 v[168:171], v250 offset:55296
	ds_read_b128 v[164:167], v251 offset:53248
	ds_read_b128 v[172:175], v251 offset:55296
	buffer_load_dwordx4 v132, s[4:7], s65 offen lds
	s_mov_b32 m0, s37
	s_add_i32 s63, s63, 0x40080
	buffer_load_dwordx4 v133, s[4:7], s65 offen lds
	s_mov_b32 m0, s40
	s_nop 0
	buffer_load_dwordx4 v132, s[4:7], s63 offen lds
	s_mov_b32 m0, s41
	s_nop 0
	buffer_load_dwordx4 v133, s[4:7], s63 offen lds
	s_mov_b32 m0, s38
	s_nop 0
	buffer_load_dwordx4 v246, s[8:11], s64 offen lds
	s_mov_b32 m0, s39
	s_nop 0
	buffer_load_dwordx4 v247, s[8:11], s64 offen lds
	s_waitcnt vmcnt(8)
	s_waitcnt lgkmcnt(0)
	s_barrier
	s_setprio 1
	s_waitcnt lgkmcnt(5)
	v_mfma_f32_16x16x128_f8f6f4 v[60:63], v[0:7], v[32:39], v[60:63]
	v_mfma_f32_16x16x128_f8f6f4 v[56:59], v[16:23], v[32:39], v[56:59]
	s_waitcnt lgkmcnt(4)
	v_mfma_f32_16x16x128_f8f6f4 v[44:47], v[0:7], v[152:159], v[184:187]
	v_mfma_f32_16x16x128_f8f6f4 v[40:43], v[16:23], v[152:159], v[188:191]
	s_waitcnt lgkmcnt(1)
	v_mfma_f32_16x16x128_f8f6f4 v[28:31], v[0:7], v[160:167], v[192:195]
	v_mfma_f32_16x16x128_f8f6f4 v[24:27], v[16:23], v[160:167], v[196:199]
	s_waitcnt lgkmcnt(0)
	v_mfma_f32_16x16x128_f8f6f4 v[12:15], v[0:7], v[168:175], v[212:215]
	v_mfma_f32_16x16x128_f8f6f4 v[8:11], v[16:23], v[168:175], v[216:219]
	s_setprio 0
	s_setprio 1
	v_mfma_f32_16x16x128_f8f6f4 v[52:55], v[136:143], v[32:39], v[52:55]
	v_mfma_f32_16x16x128_f8f6f4 v[48:51], v[144:151], v[32:39], v[48:51]
	v_mfma_f32_16x16x128_f8f6f4 v[36:39], v[136:143], v[152:159], v[220:223]
	v_mfma_f32_16x16x128_f8f6f4 v[32:35], v[144:151], v[152:159], v[224:227]
	v_mfma_f32_16x16x128_f8f6f4 v[20:23], v[136:143], v[160:167], v[228:231]
	v_mfma_f32_16x16x128_f8f6f4 v[16:19], v[144:151], v[160:167], v[232:235]
	v_mfma_f32_16x16x128_f8f6f4 v[4:7], v[136:143], v[168:175], v[236:239]
	v_mfma_f32_16x16x128_f8f6f4 v[0:3], v[144:151], v[168:175], v[240:243]
	s_setprio 0
	s_barrier
	s_add_i32 s61, s61, 2
	s_addk_i32 s62, 0x100
	s_cmp_gt_u32 s61, 13
	s_cbranch_scc1 .LBB0_2177

.LBB0_2197:
	s_cmpk_lg_i32 s64, 0x180
	s_cbranch_scc1 .Lp6_fast
	v_add_u32_e32 v129, s19, v128
	v_ashrrev_i32_e32 v131, 3, v129
	v_lshlrev_b32_e32 v130, 4, v128
	v_lshlrev_b32_e32 v132, 1, v131
	v_lshrrev_b32_e32 v133, 2, v131
	v_bitop3_b32 v130, v129, s24, v130 bitop3:0x48
	v_and_b32_e32 v132, 24, v132
	v_and_b32_e32 v133, 4, v133
	v_and_b32_e32 v134, 0x1fffe3, v131
	v_lshl_add_u32 v129, v129, 4, v156
	v_or3_b32 v132, v134, v133, v132
	v_ashrrev_i32_e32 v129, 7, v129
	v_lshl_or_b32 v159, v132, 11, v130
	v_lshlrev_b32_e32 v132, 1, v129
	v_lshrrev_b32_e32 v133, 2, v129
	v_and_b32_e32 v132, 24, v132
	v_and_b32_e32 v133, 4, v133
	v_and_b32_e32 v134, 0x1fffe3, v129
	v_or3_b32 v132, v134, v133, v132
	v_lshrrev_b32_e32 v133, 3, v128
	v_lshl_or_b32 v244, v132, 11, v130
	v_and_b32_e32 v132, 15, v128
	v_and_b32_e32 v134, 0xffffffe, v133
	v_bfe_u32 v128, v128, 1, 3
	v_lshlrev_b32_e32 v132, 7, v132
	v_bitop3_b32 v133, v133, v128, s50 bitop3:0x6c
	v_bitop3_b32 v128, v134, v128, 1 bitop3:0x36
	v_or_b32_e32 v152, s44, v132
	v_or_b32_e32 v132, s45, v132
	v_lshlrev_b32_e32 v153, 4, v133
	v_lshlrev_b32_e32 v154, 4, v128
	v_add_u32_e32 v245, v153, v132
	v_add_u32_e32 v246, v154, v132
	v_add_u32_e32 v132, s51, v245
	v_add_u32_e32 v140, s51, v246
	v_add_u32_e32 v148, s52, v245
	v_lshl_or_b32 v247, v131, 11, v130
	v_lshl_or_b32 v248, v129, 11, v130
	v_add_u32_e32 v249, 0x40000, v247
	v_add_u32_e32 v250, 0x40000, v248
	v_add3_u32 v251, v153, v152, 0
	v_add3_u32 v252, v154, v152, 0
	s_branch .Lp6_join
.Lp6_fast:
	v_add_u32_e32 v132, s51, v245
	v_add_u32_e32 v140, s51, v246
	v_add_u32_e32 v148, s52, v245
.Lp6_join:
	ds_read_b128 v[128:131], v132
	ds_read_b128 v[136:139], v132 offset:2048
	ds_read_b128 v[132:135], v140
	ds_read_b128 v[140:143], v140 offset:2048
	v_add_u32_e32 v155, s52, v246
	ds_read_b128 v[144:147], v148
	ds_read_b128 v[160:163], v148 offset:2048
	ds_read_b128 v[148:151], v155
	ds_read_b128 v[164:167], v155 offset:2048
	s_add_i32 s6, s64, 0xffffff80
	s_add_i32 s7, s6, s59
	s_cmpk_eq_i32 s64, 0x880
	s_cselect_b32 s67, s37, s56
	s_cselect_b32 s6, 0, s6
	s_cselect_b32 s66, 0x80, s64
	s_cselect_b32 s65, s31, s7
	s_add_i32 s7, s56, s64
	s_add_i32 s66, s67, s66
	s_addk_i32 s7, 0xff00
	s_add_i32 s67, s67, s6
	s_mov_b32 m0, s46
	ds_read_b128 v[168:171], v251
	ds_read_b128 v[176:179], v251 offset:2048
	ds_read_b128 v[172:175], v252
	ds_read_b128 v[180:183], v252 offset:2048
	ds_read_b128 v[184:187], v251 offset:4096
	ds_read_b128 v[192:195], v251 offset:6144
	ds_read_b128 v[188:191], v252 offset:4096
	ds_read_b128 v[196:199], v252 offset:6144
	buffer_load_dwordx4 v249, s[8:11], s7 offen lds
	s_mov_b32 m0, s49
	s_nop 0
	buffer_load_dwordx4 v250, s[8:11], s7 offen lds
	s_waitcnt vmcnt(8)
	s_waitcnt lgkmcnt(0)
	s_barrier
	s_setprio 1
	s_waitcnt lgkmcnt(5)
	v_mfma_f32_16x16x128_f8f6f4 v[124:127], v[128:135], v[168:175], v[124:127]
	v_mfma_f32_16x16x128_f8f6f4 v[120:123], v[136:143], v[168:175], v[120:123]
	s_waitcnt lgkmcnt(4)
	v_mfma_f32_16x16x128_f8f6f4 v[108:111], v[128:135], v[176:183], v[108:111]
	v_mfma_f32_16x16x128_f8f6f4 v[104:107], v[136:143], v[176:183], v[104:107]
	s_waitcnt lgkmcnt(1)
	v_mfma_f32_16x16x128_f8f6f4 v[152:155], v[128:135], v[184:191], v[92:95]
	v_mfma_f32_16x16x128_f8f6f4 v[200:203], v[136:143], v[184:191], v[88:91]
	s_waitcnt lgkmcnt(0)
	v_mfma_f32_16x16x128_f8f6f4 v[204:207], v[128:135], v[192:199], v[76:79]
	v_mfma_f32_16x16x128_f8f6f4 v[208:211], v[136:143], v[192:199], v[72:75]
	s_setprio 0
	s_setprio 1
	v_mfma_f32_16x16x128_f8f6f4 v[116:119], v[144:151], v[168:175], v[116:119]
	v_mfma_f32_16x16x128_f8f6f4 v[112:115], v[160:167], v[168:175], v[112:115]
	v_mfma_f32_16x16x128_f8f6f4 v[100:103], v[144:151], v[176:183], v[100:103]
	v_mfma_f32_16x16x128_f8f6f4 v[96:99], v[160:167], v[176:183], v[96:99]
	v_mfma_f32_16x16x128_f8f6f4 v[168:171], v[144:151], v[184:191], v[84:87]
	v_mfma_f32_16x16x128_f8f6f4 v[172:175], v[160:167], v[184:191], v[80:83]
	v_mfma_f32_16x16x128_f8f6f4 v[176:179], v[144:151], v[192:199], v[68:71]
	v_mfma_f32_16x16x128_f8f6f4 v[180:183], v[160:167], v[192:199], v[64:67]
	s_setprio 0
	s_barrier
	s_mov_b32 m0, s28
	s_mov_b32 s6, s10
	s_mov_b32 s7, s11
	s_nop 1
	ds_read_b128 v[64:67], v251 offset:16384
	ds_read_b128 v[72:75], v251 offset:18432
	ds_read_b128 v[68:71], v252 offset:16384
	ds_read_b128 v[76:79], v252 offset:18432
	ds_read_b128 v[80:83], v251 offset:20480
	ds_read_b128 v[88:91], v251 offset:22528
	ds_read_b128 v[84:87], v252 offset:20480
	ds_read_b128 v[92:95], v252 offset:22528
	buffer_load_dwordx4 v159, s[4:7], s65 offen lds
	s_mov_b32 m0, s29
	s_add_i32 s68, s65, 0x40000
	buffer_load_dwordx4 v244, s[4:7], s65 offen lds
	s_mov_b32 m0, s30
	s_nop 0
	buffer_load_dwordx4 v159, s[4:7], s68 offen lds
	s_mov_b32 m0, s33
	s_nop 0
	buffer_load_dwordx4 v244, s[4:7], s68 offen lds
	s_mov_b32 m0, s27
	s_nop 0
	buffer_load_dwordx4 v247, s[8:11], s67 offen lds
	s_mov_b32 m0, s34
	s_nop 0
	buffer_load_dwordx4 v248, s[8:11], s67 offen lds
	s_waitcnt vmcnt(8)
	s_waitcnt lgkmcnt(0)
	s_barrier
	s_setprio 1
	s_waitcnt lgkmcnt(5)
	v_mfma_f32_16x16x128_f8f6f4 v[60:63], v[128:135], v[64:71], v[60:63]
	v_mfma_f32_16x16x128_f8f6f4 v[56:59], v[136:143], v[64:71], v[56:59]
	s_waitcnt lgkmcnt(4)
	v_mfma_f32_16x16x128_f8f6f4 v[184:187], v[128:135], v[72:79], v[44:47]
	v_mfma_f32_16x16x128_f8f6f4 v[188:191], v[136:143], v[72:79], v[40:43]
	s_waitcnt lgkmcnt(1)
	v_mfma_f32_16x16x128_f8f6f4 v[192:195], v[128:135], v[80:87], v[28:31]
	v_mfma_f32_16x16x128_f8f6f4 v[196:199], v[136:143], v[80:87], v[24:27]
	s_waitcnt lgkmcnt(0)
	v_mfma_f32_16x16x128_f8f6f4 v[212:215], v[128:135], v[88:95], v[12:15]
	v_mfma_f32_16x16x128_f8f6f4 v[216:219], v[136:143], v[88:95], v[8:11]
	s_setprio 0
	s_setprio 1
	v_mfma_f32_16x16x128_f8f6f4 v[52:55], v[144:151], v[64:71], v[52:55]
	v_mfma_f32_16x16x128_f8f6f4 v[48:51], v[160:167], v[64:71], v[48:51]
	v_mfma_f32_16x16x128_f8f6f4 v[220:223], v[144:151], v[72:79], v[36:39]
	v_mfma_f32_16x16x128_f8f6f4 v[224:227], v[160:167], v[72:79], v[32:35]
	v_mfma_f32_16x16x128_f8f6f4 v[228:231], v[144:151], v[80:87], v[20:23]
	v_mfma_f32_16x16x128_f8f6f4 v[232:235], v[160:167], v[80:87], v[16:19]
	v_mfma_f32_16x16x128_f8f6f4 v[236:239], v[144:151], v[88:95], v[4:7]
	v_mfma_f32_16x16x128_f8f6f4 v[240:243], v[160:167], v[88:95], v[0:3]
	s_setprio 0
	s_barrier
	s_add_i32 s68, 0, 0x18000
	s_nop 2
	v_add_u32_e32 v4, s68, v245
	v_add_u32_e32 v8, s68, v246
	s_add_i32 s68, 0, 0x1c000
	ds_read_b128 v[0:3], v4
	ds_read_b128 v[16:19], v4 offset:2048
	ds_read_b128 v[4:7], v8
	ds_read_b128 v[20:23], v8 offset:2048
	v_add_u32_e32 v8, s68, v245
	v_add_u32_e32 v9, s68, v246
	ds_read_b128 v[128:131], v8
	ds_read_b128 v[136:139], v8 offset:2048
	ds_read_b128 v[132:135], v9
	ds_read_b128 v[140:143], v9 offset:2048
	s_mov_b32 m0, s35
	ds_read_b128 v[8:11], v251 offset:32768
	ds_read_b128 v[24:27], v251 offset:34816
	ds_read_b128 v[12:15], v252 offset:32768
	ds_read_b128 v[28:31], v252 offset:34816
	ds_read_b128 v[32:35], v251 offset:36864
	ds_read_b128 v[40:43], v251 offset:38912
	ds_read_b128 v[36:39], v252 offset:36864
	ds_read_b128 v[44:47], v252 offset:38912
	buffer_load_dwordx4 v249, s[8:11], s67 offen lds
	s_mov_b32 m0, s36
	s_nop 0
	buffer_load_dwordx4 v250, s[8:11], s67 offen lds
	s_waitcnt vmcnt(8)
	s_waitcnt lgkmcnt(0)
	s_barrier
	s_setprio 1
	s_waitcnt lgkmcnt(5)
	v_mfma_f32_16x16x128_f8f6f4 v[124:127], v[0:7], v[8:15], v[124:127]
	v_mfma_f32_16x16x128_f8f6f4 v[120:123], v[16:23], v[8:15], v[120:123]
	s_waitcnt lgkmcnt(4)
	v_mfma_f32_16x16x128_f8f6f4 v[108:111], v[0:7], v[24:31], v[108:111]
	v_mfma_f32_16x16x128_f8f6f4 v[104:107], v[16:23], v[24:31], v[104:107]
	s_waitcnt lgkmcnt(1)
	v_mfma_f32_16x16x128_f8f6f4 v[92:95], v[0:7], v[32:39], v[152:155]
	v_mfma_f32_16x16x128_f8f6f4 v[88:91], v[16:23], v[32:39], v[200:203]
	s_waitcnt lgkmcnt(0)
	v_mfma_f32_16x16x128_f8f6f4 v[76:79], v[0:7], v[40:47], v[204:207]
	v_mfma_f32_16x16x128_f8f6f4 v[72:75], v[16:23], v[40:47], v[208:211]
	s_setprio 0
	s_setprio 1
	v_mfma_f32_16x16x128_f8f6f4 v[116:119], v[128:135], v[8:15], v[116:119]
	v_mfma_f32_16x16x128_f8f6f4 v[112:115], v[136:143], v[8:15], v[112:115]
	v_mfma_f32_16x16x128_f8f6f4 v[100:103], v[128:135], v[24:31], v[100:103]
	v_mfma_f32_16x16x128_f8f6f4 v[96:99], v[136:143], v[24:31], v[96:99]
	v_mfma_f32_16x16x128_f8f6f4 v[84:87], v[128:135], v[32:39], v[168:171]
	v_mfma_f32_16x16x128_f8f6f4 v[80:83], v[136:143], v[32:39], v[172:175]
	v_mfma_f32_16x16x128_f8f6f4 v[68:71], v[128:135], v[40:47], v[176:179]
	v_mfma_f32_16x16x128_f8f6f4 v[64:67], v[136:143], v[40:47], v[180:183]
	s_setprio 0
	s_barrier
	s_mov_b32 m0, s38
	s_add_i32 s67, s65, 0x80
	ds_read_b128 v[32:35], v251 offset:49152
	ds_read_b128 v[144:147], v251 offset:51200
	ds_read_b128 v[36:39], v252 offset:49152
	ds_read_b128 v[148:151], v252 offset:51200
	ds_read_b128 v[160:163], v251 offset:53248
	ds_read_b128 v[168:171], v251 offset:55296
	ds_read_b128 v[164:167], v252 offset:53248
	ds_read_b128 v[172:175], v252 offset:55296
	buffer_load_dwordx4 v159, s[4:7], s67 offen lds
	s_mov_b32 m0, s39
	s_add_i32 s65, s65, 0x40080
	buffer_load_dwordx4 v244, s[4:7], s67 offen lds
	s_mov_b32 m0, s42
	s_nop 0
	buffer_load_dwordx4 v159, s[4:7], s65 offen lds
	s_mov_b32 m0, s43
	s_nop 0
	buffer_load_dwordx4 v244, s[4:7], s65 offen lds
	s_mov_b32 m0, s40
	s_nop 0
	buffer_load_dwordx4 v247, s[8:11], s66 offen lds
	s_mov_b32 m0, s41
	s_nop 0
	buffer_load_dwordx4 v248, s[8:11], s66 offen lds
	s_waitcnt vmcnt(8)
	s_waitcnt lgkmcnt(0)
	s_barrier
	s_setprio 1
	s_waitcnt lgkmcnt(5)
	v_mfma_f32_16x16x128_f8f6f4 v[60:63], v[0:7], v[32:39], v[60:63]
	v_mfma_f32_16x16x128_f8f6f4 v[56:59], v[16:23], v[32:39], v[56:59]
	s_waitcnt lgkmcnt(4)
	v_mfma_f32_16x16x128_f8f6f4 v[44:47], v[0:7], v[144:151], v[184:187]
	v_mfma_f32_16x16x128_f8f6f4 v[40:43], v[16:23], v[144:151], v[188:191]
	s_waitcnt lgkmcnt(1)
	v_mfma_f32_16x16x128_f8f6f4 v[28:31], v[0:7], v[160:167], v[192:195]
	v_mfma_f32_16x16x128_f8f6f4 v[24:27], v[16:23], v[160:167], v[196:199]
	s_waitcnt lgkmcnt(0)
	v_mfma_f32_16x16x128_f8f6f4 v[12:15], v[0:7], v[168:175], v[212:215]
	v_mfma_f32_16x16x128_f8f6f4 v[8:11], v[16:23], v[168:175], v[216:219]
	s_setprio 0
	s_setprio 1
	v_mfma_f32_16x16x128_f8f6f4 v[52:55], v[128:135], v[32:39], v[52:55]
	v_mfma_f32_16x16x128_f8f6f4 v[48:51], v[136:143], v[32:39], v[48:51]
	v_mfma_f32_16x16x128_f8f6f4 v[36:39], v[128:135], v[144:151], v[220:223]
	v_mfma_f32_16x16x128_f8f6f4 v[32:35], v[136:143], v[144:151], v[224:227]
	v_mfma_f32_16x16x128_f8f6f4 v[20:23], v[128:135], v[160:167], v[228:231]
	v_mfma_f32_16x16x128_f8f6f4 v[16:19], v[136:143], v[160:167], v[232:235]
	v_mfma_f32_16x16x128_f8f6f4 v[4:7], v[128:135], v[168:175], v[236:239]
	v_mfma_f32_16x16x128_f8f6f4 v[0:3], v[136:143], v[168:175], v[240:243]
	s_setprio 0
	s_barrier
	s_add_i32 s63, s63, 2
	s_addk_i32 s64, 0x100
	s_cmp_gt_u32 s63, 13
	s_cbranch_scc1 .LBB0_2201

.LBB0_2275:
	s_cmpk_lg_i32 s61, 0x180
	s_cbranch_scc1 .Lp7_fast
	v_add_u32_e32 v129, s17, v128
	v_ashrrev_i32_e32 v131, 3, v129
	v_lshlrev_b32_e32 v130, 4, v128
	v_lshlrev_b32_e32 v132, 1, v131
	v_lshrrev_b32_e32 v133, 2, v131
	v_bitop3_b32 v130, v129, s22, v130 bitop3:0x48
	v_and_b32_e32 v132, 24, v132
	v_and_b32_e32 v133, 4, v133
	v_and_b32_e32 v134, 0x1fffe3, v131
	v_lshl_add_u32 v129, v129, 4, v136
	v_or3_b32 v132, v134, v133, v132
	v_ashrrev_i32_e32 v129, 7, v129
	v_lshl_or_b32 v242, v132, 11, v130
	v_lshlrev_b32_e32 v132, 1, v129
	v_lshrrev_b32_e32 v133, 2, v129
	v_and_b32_e32 v132, 24, v132
	v_and_b32_e32 v133, 4, v133
	v_and_b32_e32 v134, 0x1fffe3, v129
	v_or3_b32 v132, v134, v133, v132
	v_lshrrev_b32_e32 v133, 3, v128
	v_lshl_or_b32 v243, v132, 11, v130
	v_and_b32_e32 v132, 15, v128
	v_and_b32_e32 v134, 0xffffffe, v133
	v_bfe_u32 v128, v128, 1, 3
	v_lshlrev_b32_e32 v132, 7, v132
	v_bitop3_b32 v133, v133, v128, s48 bitop3:0x6c
	v_bitop3_b32 v128, v134, v128, 1 bitop3:0x36
	v_or_b32_e32 v162, s42, v132
	v_or_b32_e32 v132, s43, v132
	v_lshlrev_b32_e32 v163, 4, v133
	v_lshlrev_b32_e32 v164, 4, v128
	v_add_u32_e32 v244, v163, v132
	v_add_u32_e32 v245, v164, v132
	v_add_u32_e32 v132, s49, v244
	v_add_u32_e32 v142, s49, v245
	v_add_u32_e32 v150, s50, v244
	v_add_u32_e32 v158, s50, v245
	v_lshl_or_b32 v246, v131, 11, v130
	v_lshl_or_b32 v247, v129, 11, v130
	v_add_u32_e32 v248, 0x40000, v246
	v_add_u32_e32 v249, 0x40000, v247
	v_add3_u32 v250, v163, v162, 0
	v_add3_u32 v251, v164, v162, 0
	s_branch .Lp7_join
.Lp7_fast:
	v_add_u32_e32 v132, s49, v244
	v_add_u32_e32 v142, s49, v245
	v_add_u32_e32 v150, s50, v244
	v_add_u32_e32 v158, s50, v245
.Lp7_join:
	ds_read_b128 v[128:131], v132
	ds_read_b128 v[138:141], v132 offset:2048
	ds_read_b128 v[132:135], v142
	ds_read_b128 v[142:145], v142 offset:2048
	ds_read_b128 v[146:149], v150
	ds_read_b128 v[154:157], v150 offset:2048
	ds_read_b128 v[150:153], v158
	ds_read_b128 v[158:161], v158 offset:2048
	s_add_i32 s6, s61, 0xffffff80
	s_add_i32 s7, s6, s56
	s_cmpk_eq_i32 s61, 0x880
	s_cselect_b32 s64, s35, s53
	s_cselect_b32 s6, 0, s6
	s_cselect_b32 s63, 0x80, s61
	s_cselect_b32 s62, s29, s7
	s_add_i32 s7, s53, s61
	s_add_i32 s63, s64, s63
	s_addk_i32 s7, 0xff00
	s_add_i32 s64, s64, s6
	s_mov_b32 m0, s44
	ds_read_b128 v[162:165], v250
	ds_read_b128 v[170:173], v250 offset:2048
	ds_read_b128 v[166:169], v251
	ds_read_b128 v[174:177], v251 offset:2048
	ds_read_b128 v[178:181], v250 offset:4096
	ds_read_b128 v[186:189], v250 offset:6144
	ds_read_b128 v[182:185], v251 offset:4096
	ds_read_b128 v[190:193], v251 offset:6144
	buffer_load_dwordx4 v248, s[8:11], s7 offen lds
	s_mov_b32 m0, s47
	s_nop 0
	buffer_load_dwordx4 v249, s[8:11], s7 offen lds
	s_waitcnt vmcnt(8)
	s_waitcnt lgkmcnt(0)
	s_barrier
	s_setprio 1
	s_waitcnt lgkmcnt(0)
	v_mfma_f32_16x16x128_f8f6f4 v[124:127], v[128:135], v[162:169], v[124:127]
	v_mfma_f32_16x16x128_f8f6f4 v[120:123], v[138:145], v[162:169], v[120:123]
	v_mfma_f32_16x16x128_f8f6f4 v[116:119], v[128:135], v[170:177], v[116:119]
	v_mfma_f32_16x16x128_f8f6f4 v[112:115], v[138:145], v[170:177], v[112:115]
	v_mfma_f32_16x16x128_f8f6f4 v[194:197], v[128:135], v[178:185], v[92:95]
	v_mfma_f32_16x16x128_f8f6f4 v[198:201], v[138:145], v[178:185], v[88:91]
	v_mfma_f32_16x16x128_f8f6f4 v[202:205], v[128:135], v[186:193], v[84:87]
	v_mfma_f32_16x16x128_f8f6f4 v[206:209], v[138:145], v[186:193], v[80:83]
	s_setprio 0
	s_setprio 1
	v_mfma_f32_16x16x128_f8f6f4 v[108:111], v[146:153], v[162:169], v[108:111]
	v_mfma_f32_16x16x128_f8f6f4 v[104:107], v[154:161], v[162:169], v[104:107]
	v_mfma_f32_16x16x128_f8f6f4 v[100:103], v[146:153], v[170:177], v[100:103]
	v_mfma_f32_16x16x128_f8f6f4 v[96:99], v[154:161], v[170:177], v[96:99]
	v_mfma_f32_16x16x128_f8f6f4 v[162:165], v[146:153], v[178:185], v[76:79]
	v_mfma_f32_16x16x128_f8f6f4 v[166:169], v[154:161], v[178:185], v[72:75]
	v_mfma_f32_16x16x128_f8f6f4 v[170:173], v[146:153], v[186:193], v[68:71]
	v_mfma_f32_16x16x128_f8f6f4 v[174:177], v[154:161], v[186:193], v[64:67]
	s_setprio 0
	s_barrier
	s_mov_b32 m0, s26
	s_mov_b32 s6, s10
	s_mov_b32 s7, s11
	s_nop 1
	ds_read_b128 v[64:67], v250 offset:16384
	ds_read_b128 v[72:75], v250 offset:18432
	ds_read_b128 v[68:71], v251 offset:16384
	ds_read_b128 v[76:79], v251 offset:18432
	ds_read_b128 v[80:83], v250 offset:20480
	ds_read_b128 v[88:91], v250 offset:22528
	ds_read_b128 v[84:87], v251 offset:20480
	ds_read_b128 v[92:95], v251 offset:22528
	buffer_load_dwordx4 v242, s[4:7], s62 offen lds
	s_mov_b32 m0, s27
	s_add_i32 s65, s62, 0x40000
	buffer_load_dwordx4 v243, s[4:7], s62 offen lds
	s_mov_b32 m0, s28
	s_nop 0
	buffer_load_dwordx4 v242, s[4:7], s65 offen lds
	s_mov_b32 m0, s30
	s_nop 0
	buffer_load_dwordx4 v243, s[4:7], s65 offen lds
	s_mov_b32 m0, s25
	s_nop 0
	buffer_load_dwordx4 v246, s[8:11], s64 offen lds
	s_mov_b32 m0, s31
	s_nop 0
	buffer_load_dwordx4 v247, s[8:11], s64 offen lds
	s_waitcnt vmcnt(8)
	s_waitcnt lgkmcnt(0)
	s_barrier
	s_setprio 1
	s_waitcnt lgkmcnt(5)
	v_mfma_f32_16x16x128_f8f6f4 v[60:63], v[128:135], v[64:71], v[60:63]
	v_mfma_f32_16x16x128_f8f6f4 v[56:59], v[138:145], v[64:71], v[56:59]
	s_waitcnt lgkmcnt(4)
	v_mfma_f32_16x16x128_f8f6f4 v[52:55], v[128:135], v[72:79], v[52:55]
	v_mfma_f32_16x16x128_f8f6f4 v[48:51], v[138:145], v[72:79], v[48:51]
	s_waitcnt lgkmcnt(1)
	v_mfma_f32_16x16x128_f8f6f4 v[178:181], v[128:135], v[80:87], v[28:31]
	v_mfma_f32_16x16x128_f8f6f4 v[182:185], v[138:145], v[80:87], v[24:27]
	s_waitcnt lgkmcnt(0)
	v_mfma_f32_16x16x128_f8f6f4 v[186:189], v[128:135], v[88:95], v[20:23]
	v_mfma_f32_16x16x128_f8f6f4 v[190:193], v[138:145], v[88:95], v[16:19]
	s_setprio 0
	s_setprio 1
	v_mfma_f32_16x16x128_f8f6f4 v[210:213], v[146:153], v[64:71], v[44:47]
	v_mfma_f32_16x16x128_f8f6f4 v[214:217], v[154:161], v[64:71], v[40:43]
	v_mfma_f32_16x16x128_f8f6f4 v[218:221], v[146:153], v[72:79], v[36:39]
	v_mfma_f32_16x16x128_f8f6f4 v[222:225], v[154:161], v[72:79], v[32:35]
	v_mfma_f32_16x16x128_f8f6f4 v[226:229], v[146:153], v[80:87], v[12:15]
	v_mfma_f32_16x16x128_f8f6f4 v[230:233], v[154:161], v[80:87], v[8:11]
	v_mfma_f32_16x16x128_f8f6f4 v[234:237], v[146:153], v[88:95], v[4:7]
	v_mfma_f32_16x16x128_f8f6f4 v[238:241], v[154:161], v[88:95], v[0:3]
	s_setprio 0
	s_barrier
	s_add_i32 s65, 0, 0x18000
	s_nop 2
	v_add_u32_e32 v4, s65, v244
	v_add_u32_e32 v12, s65, v245
	s_add_i32 s65, 0, 0x1c000
	v_add_u32_e32 v16, s65, v244
	ds_read_b128 v[0:3], v4
	ds_read_b128 v[8:11], v4 offset:2048
	ds_read_b128 v[4:7], v12
	ds_read_b128 v[12:15], v12 offset:2048
	v_add_u32_e32 v17, s65, v245
	ds_read_b128 v[128:131], v16
	ds_read_b128 v[138:141], v16 offset:2048
	ds_read_b128 v[132:135], v17
	ds_read_b128 v[142:145], v17 offset:2048
	s_mov_b32 m0, s33
	ds_read_b128 v[16:19], v250 offset:32768
	ds_read_b128 v[24:27], v250 offset:34816
	ds_read_b128 v[20:23], v251 offset:32768
	ds_read_b128 v[28:31], v251 offset:34816
	ds_read_b128 v[32:35], v250 offset:36864
	ds_read_b128 v[40:43], v250 offset:38912
	ds_read_b128 v[36:39], v251 offset:36864
	ds_read_b128 v[44:47], v251 offset:38912
	buffer_load_dwordx4 v248, s[8:11], s64 offen lds
	s_mov_b32 m0, s34
	s_nop 0
	buffer_load_dwordx4 v249, s[8:11], s64 offen lds
	s_waitcnt vmcnt(8)
	s_waitcnt lgkmcnt(0)
	s_barrier
	s_setprio 1
	s_waitcnt lgkmcnt(5)
	v_mfma_f32_16x16x128_f8f6f4 v[124:127], v[0:7], v[16:23], v[124:127]
	v_mfma_f32_16x16x128_f8f6f4 v[120:123], v[8:15], v[16:23], v[120:123]
	s_waitcnt lgkmcnt(4)
	v_mfma_f32_16x16x128_f8f6f4 v[116:119], v[0:7], v[24:31], v[116:119]
	v_mfma_f32_16x16x128_f8f6f4 v[112:115], v[8:15], v[24:31], v[112:115]
	s_waitcnt lgkmcnt(1)
	v_mfma_f32_16x16x128_f8f6f4 v[92:95], v[0:7], v[32:39], v[194:197]
	v_mfma_f32_16x16x128_f8f6f4 v[88:91], v[8:15], v[32:39], v[198:201]
	s_waitcnt lgkmcnt(0)
	v_mfma_f32_16x16x128_f8f6f4 v[84:87], v[0:7], v[40:47], v[202:205]
	v_mfma_f32_16x16x128_f8f6f4 v[80:83], v[8:15], v[40:47], v[206:209]
	s_setprio 0
	s_setprio 1
	v_mfma_f32_16x16x128_f8f6f4 v[108:111], v[128:135], v[16:23], v[108:111]
	v_mfma_f32_16x16x128_f8f6f4 v[104:107], v[138:145], v[16:23], v[104:107]
	v_mfma_f32_16x16x128_f8f6f4 v[100:103], v[128:135], v[24:31], v[100:103]
	v_mfma_f32_16x16x128_f8f6f4 v[96:99], v[138:145], v[24:31], v[96:99]
	v_mfma_f32_16x16x128_f8f6f4 v[76:79], v[128:135], v[32:39], v[162:165]
	v_mfma_f32_16x16x128_f8f6f4 v[72:75], v[138:145], v[32:39], v[166:169]
	v_mfma_f32_16x16x128_f8f6f4 v[68:71], v[128:135], v[40:47], v[170:173]
	v_mfma_f32_16x16x128_f8f6f4 v[64:67], v[138:145], v[40:47], v[174:177]
	s_setprio 0
	s_barrier
	s_mov_b32 m0, s36
	s_add_i32 s64, s62, 0x80
	ds_read_b128 v[32:35], v250 offset:49152
	ds_read_b128 v[146:149], v250 offset:51200
	ds_read_b128 v[36:39], v251 offset:49152
	ds_read_b128 v[150:153], v251 offset:51200
	ds_read_b128 v[154:157], v250 offset:53248
	ds_read_b128 v[162:165], v250 offset:55296
	ds_read_b128 v[158:161], v251 offset:53248
	ds_read_b128 v[166:169], v251 offset:55296
	buffer_load_dwordx4 v242, s[4:7], s64 offen lds
	s_mov_b32 m0, s37
	s_add_i32 s62, s62, 0x40080
	buffer_load_dwordx4 v243, s[4:7], s64 offen lds
	s_mov_b32 m0, s40
	s_nop 0
	buffer_load_dwordx4 v242, s[4:7], s62 offen lds
	s_mov_b32 m0, s41
	s_nop 0
	buffer_load_dwordx4 v243, s[4:7], s62 offen lds
	s_mov_b32 m0, s38
	s_nop 0
	buffer_load_dwordx4 v246, s[8:11], s63 offen lds
	s_mov_b32 m0, s39
	s_nop 0
	buffer_load_dwordx4 v247, s[8:11], s63 offen lds
	s_waitcnt vmcnt(8)
	s_waitcnt lgkmcnt(0)
	s_barrier
	s_setprio 1
	s_waitcnt lgkmcnt(5)
	v_mfma_f32_16x16x128_f8f6f4 v[60:63], v[0:7], v[32:39], v[60:63]
	v_mfma_f32_16x16x128_f8f6f4 v[56:59], v[8:15], v[32:39], v[56:59]
	s_waitcnt lgkmcnt(4)
	v_mfma_f32_16x16x128_f8f6f4 v[52:55], v[0:7], v[146:153], v[52:55]
	v_mfma_f32_16x16x128_f8f6f4 v[48:51], v[8:15], v[146:153], v[48:51]
	s_waitcnt lgkmcnt(1)
	v_mfma_f32_16x16x128_f8f6f4 v[28:31], v[0:7], v[154:161], v[178:181]
	v_mfma_f32_16x16x128_f8f6f4 v[24:27], v[8:15], v[154:161], v[182:185]
	s_waitcnt lgkmcnt(0)
	v_mfma_f32_16x16x128_f8f6f4 v[20:23], v[0:7], v[162:169], v[186:189]
	v_mfma_f32_16x16x128_f8f6f4 v[16:19], v[8:15], v[162:169], v[190:193]
	s_setprio 0
	s_setprio 1
	v_mfma_f32_16x16x128_f8f6f4 v[44:47], v[128:135], v[32:39], v[210:213]
	v_mfma_f32_16x16x128_f8f6f4 v[40:43], v[138:145], v[32:39], v[214:217]
	v_mfma_f32_16x16x128_f8f6f4 v[36:39], v[128:135], v[146:153], v[218:221]
	v_mfma_f32_16x16x128_f8f6f4 v[32:35], v[138:145], v[146:153], v[222:225]
	v_mfma_f32_16x16x128_f8f6f4 v[12:15], v[128:135], v[154:161], v[226:229]
	v_mfma_f32_16x16x128_f8f6f4 v[8:11], v[138:145], v[154:161], v[230:233]
	v_mfma_f32_16x16x128_f8f6f4 v[4:7], v[128:135], v[162:169], v[234:237]
	v_mfma_f32_16x16x128_f8f6f4 v[0:3], v[138:145], v[162:169], v[238:241]
	s_setprio 0
	s_barrier
	s_add_i32 s60, s60, 2
	s_addk_i32 s61, 0x100
	s_cmp_gt_u32 s60, 13
	s_cbranch_scc1 .LBB0_2279

.LBB0_2568:
	s_cmpk_lg_i32 s80, 0x180
	s_cbranch_scc1 .Lp11_fast
	v_add_u32_e32 v129, s36, v128
	v_ashrrev_i32_e32 v131, 3, v129
	v_lshlrev_b32_e32 v130, 4, v128
	v_lshlrev_b32_e32 v132, 1, v131
	v_lshrrev_b32_e32 v133, 2, v131
	v_bitop3_b32 v130, v129, s37, v130 bitop3:0x48
	v_and_b32_e32 v132, 24, v132
	v_and_b32_e32 v133, 4, v133
	v_and_b32_e32 v134, 0x1fffe3, v131
	v_lshl_add_u32 v129, v129, 4, v147
	v_or3_b32 v132, v134, v133, v132
	v_ashrrev_i32_e32 v129, 7, v129
	v_lshl_or_b32 v144, v132, 11, v130
	v_lshlrev_b32_e32 v132, 1, v129
	v_lshrrev_b32_e32 v133, 2, v129
	v_and_b32_e32 v132, 24, v132
	v_and_b32_e32 v133, 4, v133
	v_and_b32_e32 v134, 0x1fffe3, v129
	v_or3_b32 v132, v134, v133, v132
	v_lshrrev_b32_e32 v133, 3, v128
	v_lshl_or_b32 v145, v132, 11, v130
	v_and_b32_e32 v132, 15, v128
	v_and_b32_e32 v134, 0xffffffe, v133
	v_bfe_u32 v128, v128, 1, 3
	v_lshlrev_b32_e32 v132, 7, v132
	v_bitop3_b32 v133, v133, v128, s64 bitop3:0x6c
	v_bitop3_b32 v128, v134, v128, 1 bitop3:0x36
	v_or_b32_e32 v146, s58, v132
	v_or_b32_e32 v132, s59, v132
	v_lshlrev_b32_e32 v148, 4, v133
	v_lshlrev_b32_e32 v151, 4, v128
	v_add_u32_e32 v150, v148, v132
	v_add_u32_e32 v152, v151, v132
	v_add_u32_e32 v132, s65, v150
	v_add_u32_e32 v140, s65, v152
	v_add_u32_e32 v158, s66, v150
	v_add_u32_e32 v166, s66, v152
	v_lshl_or_b32 v250, v131, 11, v130
	v_lshl_or_b32 v251, v129, 11, v130
	v_add_u32_e32 v252, 0x40000, v250
	v_add_u32_e32 v253, 0x40000, v251
	v_add3_u32 v148, v148, v146, 0
	v_add3_u32 v146, v151, v146, 0
	s_branch .Lp11_join
.Lp11_fast:
	v_add_u32_e32 v132, s65, v150
	v_add_u32_e32 v140, s65, v152
	v_add_u32_e32 v158, s66, v150
	v_add_u32_e32 v166, s66, v152
.Lp11_join:
	ds_read_b128 v[128:131], v132
	ds_read_b128 v[136:139], v132 offset:2048
	ds_read_b128 v[132:135], v140
	ds_read_b128 v[140:143], v140 offset:2048
	ds_read_b128 v[154:157], v158
	ds_read_b128 v[162:165], v158 offset:2048
	ds_read_b128 v[158:161], v166
	ds_read_b128 v[166:169], v166 offset:2048
	s_add_i32 s6, s80, 0xffffff80
	s_add_i32 s7, s6, s75
	s_cmpk_eq_i32 s80, 0x880
	s_cselect_b32 s81, s71, s35
	s_cselect_b32 s11, 0x80, s80
	s_cselect_b32 s10, 0, s6
	s_cselect_b32 s6, s51, s7
	s_add_i32 s7, s81, s11
	s_add_i32 s11, s35, s80
	s_addk_i32 s11, 0xff00
	s_add_i32 s81, s81, s10
	s_mov_b32 m0, s60
	ds_read_b128 v[170:173], v148
	ds_read_b128 v[178:181], v148 offset:2048
	ds_read_b128 v[174:177], v146
	ds_read_b128 v[182:185], v146 offset:2048
	ds_read_b128 v[186:189], v148 offset:4096
	ds_read_b128 v[194:197], v148 offset:6144
	ds_read_b128 v[190:193], v146 offset:4096
	ds_read_b128 v[198:201], v146 offset:6144
	buffer_load_dwordx4 v252, s[88:91], s11 offen lds
	s_mov_b32 m0, s63
	s_nop 0
	buffer_load_dwordx4 v253, s[88:91], s11 offen lds
	s_waitcnt vmcnt(8)
	s_waitcnt lgkmcnt(0)
	s_barrier
	s_setprio 1
	s_waitcnt lgkmcnt(0)
	v_mfma_f32_16x16x128_f8f6f4 v[124:127], v[128:135], v[170:177], v[124:127]
	v_mfma_f32_16x16x128_f8f6f4 v[120:123], v[136:143], v[170:177], v[120:123]
	v_mfma_f32_16x16x128_f8f6f4 v[116:119], v[128:135], v[178:185], v[116:119]
	v_mfma_f32_16x16x128_f8f6f4 v[112:115], v[136:143], v[178:185], v[112:115]
	v_mfma_f32_16x16x128_f8f6f4 v[96:99], v[128:135], v[186:193], v[96:99]
	v_mfma_f32_16x16x128_f8f6f4 v[202:205], v[136:143], v[186:193], v[88:91]
	v_mfma_f32_16x16x128_f8f6f4 v[206:209], v[128:135], v[194:201], v[80:83]
	v_mfma_f32_16x16x128_f8f6f4 v[210:213], v[136:143], v[194:201], v[72:75]
	s_setprio 0
	s_setprio 1
	v_mfma_f32_16x16x128_f8f6f4 v[108:111], v[154:161], v[170:177], v[108:111]
	v_mfma_f32_16x16x128_f8f6f4 v[104:107], v[162:169], v[170:177], v[104:107]
	v_mfma_f32_16x16x128_f8f6f4 v[100:103], v[154:161], v[178:185], v[100:103]
	v_mfma_f32_16x16x128_f8f6f4 v[170:173], v[162:169], v[178:185], v[92:95]
	v_mfma_f32_16x16x128_f8f6f4 v[174:177], v[154:161], v[186:193], v[84:87]
	v_mfma_f32_16x16x128_f8f6f4 v[178:181], v[162:169], v[186:193], v[76:79]
	v_mfma_f32_16x16x128_f8f6f4 v[182:185], v[154:161], v[194:201], v[68:71]
	v_mfma_f32_16x16x128_f8f6f4 v[186:189], v[162:169], v[194:201], v[64:67]
	s_setprio 0
	s_barrier
	s_mov_b32 m0, s43
	s_mov_b32 s10, s90
	s_mov_b32 s11, s91
	s_nop 1
	ds_read_b128 v[64:67], v148 offset:16384
	ds_read_b128 v[72:75], v148 offset:18432
	ds_read_b128 v[68:71], v146 offset:16384
	ds_read_b128 v[76:79], v146 offset:18432
	ds_read_b128 v[80:83], v148 offset:20480
	ds_read_b128 v[88:91], v148 offset:22528
	ds_read_b128 v[84:87], v146 offset:20480
	ds_read_b128 v[92:95], v146 offset:22528
	buffer_load_dwordx4 v144, s[8:11], s6 offen lds
	s_mov_b32 m0, s44
	s_add_i32 s82, s6, 0x40000
	buffer_load_dwordx4 v145, s[8:11], s6 offen lds
	s_mov_b32 m0, s45
	s_nop 0
	buffer_load_dwordx4 v144, s[8:11], s82 offen lds
	s_mov_b32 m0, s46
	s_nop 0
	buffer_load_dwordx4 v145, s[8:11], s82 offen lds
	s_mov_b32 m0, s42
	s_nop 0
	buffer_load_dwordx4 v250, s[88:91], s81 offen lds
	s_mov_b32 m0, s47
	s_nop 0
	buffer_load_dwordx4 v251, s[88:91], s81 offen lds
	s_waitcnt vmcnt(8)
	s_waitcnt lgkmcnt(0)
	s_barrier
	s_setprio 1
	s_waitcnt lgkmcnt(5)
	v_mfma_f32_16x16x128_f8f6f4 v[60:63], v[128:135], v[64:71], v[60:63]
	v_mfma_f32_16x16x128_f8f6f4 v[56:59], v[136:143], v[64:71], v[56:59]
	s_waitcnt lgkmcnt(4)
	v_mfma_f32_16x16x128_f8f6f4 v[48:51], v[128:135], v[72:79], v[48:51]
	v_mfma_f32_16x16x128_f8f6f4 v[190:193], v[136:143], v[72:79], v[40:43]
	s_waitcnt lgkmcnt(1)
	v_mfma_f32_16x16x128_f8f6f4 v[194:197], v[128:135], v[80:87], v[32:35]
	v_mfma_f32_16x16x128_f8f6f4 v[198:201], v[136:143], v[80:87], v[24:27]
	s_waitcnt lgkmcnt(0)
	v_mfma_f32_16x16x128_f8f6f4 v[214:217], v[128:135], v[88:95], v[16:19]
	v_mfma_f32_16x16x128_f8f6f4 v[218:221], v[136:143], v[88:95], v[8:11]
	s_setprio 0
	s_setprio 1
	v_mfma_f32_16x16x128_f8f6f4 v[52:55], v[154:161], v[64:71], v[52:55]
	v_mfma_f32_16x16x128_f8f6f4 v[222:225], v[162:169], v[64:71], v[44:47]
	v_mfma_f32_16x16x128_f8f6f4 v[226:229], v[154:161], v[72:79], v[36:39]
	v_mfma_f32_16x16x128_f8f6f4 v[230:233], v[162:169], v[72:79], v[28:31]
	v_mfma_f32_16x16x128_f8f6f4 v[234:237], v[154:161], v[80:87], v[20:23]
	v_mfma_f32_16x16x128_f8f6f4 v[238:241], v[162:169], v[80:87], v[12:15]
	v_mfma_f32_16x16x128_f8f6f4 v[242:245], v[154:161], v[88:95], v[4:7]
	v_mfma_f32_16x16x128_f8f6f4 v[246:249], v[162:169], v[88:95], v[0:3]
	s_setprio 0
	s_barrier
	s_add_i32 s82, 0, 0x18000
	s_nop 2
	v_add_u32_e32 v4, s82, v150
	v_add_u32_e32 v12, s82, v152
	s_add_i32 s82, 0, 0x1c000
	v_add_u32_e32 v16, s82, v150
	ds_read_b128 v[0:3], v4
	ds_read_b128 v[8:11], v4 offset:2048
	ds_read_b128 v[4:7], v12
	ds_read_b128 v[12:15], v12 offset:2048
	v_add_u32_e32 v17, s82, v152
	ds_read_b128 v[128:131], v16
	ds_read_b128 v[136:139], v16 offset:2048
	ds_read_b128 v[132:135], v17
	ds_read_b128 v[140:143], v17 offset:2048
	s_mov_b32 m0, s48
	ds_read_b128 v[16:19], v148 offset:32768
	ds_read_b128 v[24:27], v148 offset:34816
	ds_read_b128 v[20:23], v146 offset:32768
	ds_read_b128 v[28:31], v146 offset:34816
	ds_read_b128 v[32:35], v148 offset:36864
	ds_read_b128 v[40:43], v148 offset:38912
	ds_read_b128 v[36:39], v146 offset:36864
	ds_read_b128 v[44:47], v146 offset:38912
	buffer_load_dwordx4 v252, s[88:91], s81 offen lds
	s_mov_b32 m0, s49
	s_nop 0
	buffer_load_dwordx4 v253, s[88:91], s81 offen lds
	s_waitcnt vmcnt(8)
	s_waitcnt lgkmcnt(0)
	s_barrier
	s_setprio 1
	s_waitcnt lgkmcnt(5)
	v_mfma_f32_16x16x128_f8f6f4 v[124:127], v[0:7], v[16:23], v[124:127]
	v_mfma_f32_16x16x128_f8f6f4 v[120:123], v[8:15], v[16:23], v[120:123]
	s_waitcnt lgkmcnt(4)
	v_mfma_f32_16x16x128_f8f6f4 v[116:119], v[0:7], v[24:31], v[116:119]
	v_mfma_f32_16x16x128_f8f6f4 v[112:115], v[8:15], v[24:31], v[112:115]
	s_waitcnt lgkmcnt(1)
	v_mfma_f32_16x16x128_f8f6f4 v[96:99], v[0:7], v[32:39], v[96:99]
	v_mfma_f32_16x16x128_f8f6f4 v[88:91], v[8:15], v[32:39], v[202:205]
	s_waitcnt lgkmcnt(0)
	v_mfma_f32_16x16x128_f8f6f4 v[80:83], v[0:7], v[40:47], v[206:209]
	v_mfma_f32_16x16x128_f8f6f4 v[72:75], v[8:15], v[40:47], v[210:213]
	s_setprio 0
	s_setprio 1
	v_mfma_f32_16x16x128_f8f6f4 v[108:111], v[128:135], v[16:23], v[108:111]
	v_mfma_f32_16x16x128_f8f6f4 v[104:107], v[136:143], v[16:23], v[104:107]
	v_mfma_f32_16x16x128_f8f6f4 v[100:103], v[128:135], v[24:31], v[100:103]
	v_mfma_f32_16x16x128_f8f6f4 v[92:95], v[136:143], v[24:31], v[170:173]
	v_mfma_f32_16x16x128_f8f6f4 v[84:87], v[128:135], v[32:39], v[174:177]
	v_mfma_f32_16x16x128_f8f6f4 v[76:79], v[136:143], v[32:39], v[178:181]
	v_mfma_f32_16x16x128_f8f6f4 v[68:71], v[128:135], v[40:47], v[182:185]
	v_mfma_f32_16x16x128_f8f6f4 v[64:67], v[136:143], v[40:47], v[186:189]
	s_setprio 0
	s_barrier
	s_mov_b32 m0, s52
	s_add_i32 s81, s6, 0x80
	ds_read_b128 v[154:157], v148 offset:49152
	ds_read_b128 v[162:165], v148 offset:51200
	ds_read_b128 v[158:161], v146 offset:49152
	ds_read_b128 v[166:169], v146 offset:51200
	ds_read_b128 v[170:173], v148 offset:53248
	ds_read_b128 v[178:181], v148 offset:55296
	ds_read_b128 v[174:177], v146 offset:53248
	ds_read_b128 v[182:185], v146 offset:55296
	buffer_load_dwordx4 v144, s[8:11], s81 offen lds
	s_mov_b32 m0, s53
	s_add_i32 s6, s6, 0x40080
	buffer_load_dwordx4 v145, s[8:11], s81 offen lds
	s_mov_b32 m0, s56
	s_nop 0
	buffer_load_dwordx4 v144, s[8:11], s6 offen lds
	s_mov_b32 m0, s57
	s_nop 0
	buffer_load_dwordx4 v145, s[8:11], s6 offen lds
	s_mov_b32 m0, s54
	s_nop 0
	buffer_load_dwordx4 v250, s[88:91], s7 offen lds
	s_mov_b32 m0, s55
	s_nop 0
	buffer_load_dwordx4 v251, s[88:91], s7 offen lds
	s_waitcnt vmcnt(8)
	s_waitcnt lgkmcnt(0)
	s_barrier
	s_setprio 1
	s_waitcnt lgkmcnt(5)
	v_mfma_f32_16x16x128_f8f6f4 v[60:63], v[0:7], v[154:161], v[60:63]
	v_mfma_f32_16x16x128_f8f6f4 v[56:59], v[8:15], v[154:161], v[56:59]
	s_waitcnt lgkmcnt(4)
	v_mfma_f32_16x16x128_f8f6f4 v[48:51], v[0:7], v[162:169], v[48:51]
	v_mfma_f32_16x16x128_f8f6f4 v[40:43], v[8:15], v[162:169], v[190:193]
	s_waitcnt lgkmcnt(1)
	v_mfma_f32_16x16x128_f8f6f4 v[32:35], v[0:7], v[170:177], v[194:197]
	v_mfma_f32_16x16x128_f8f6f4 v[24:27], v[8:15], v[170:177], v[198:201]
	s_waitcnt lgkmcnt(0)
	v_mfma_f32_16x16x128_f8f6f4 v[16:19], v[0:7], v[178:185], v[214:217]
	v_mfma_f32_16x16x128_f8f6f4 v[8:11], v[8:15], v[178:185], v[218:221]
	s_setprio 0
	s_setprio 1
	v_mfma_f32_16x16x128_f8f6f4 v[52:55], v[128:135], v[154:161], v[52:55]
	v_mfma_f32_16x16x128_f8f6f4 v[44:47], v[136:143], v[154:161], v[222:225]
	v_mfma_f32_16x16x128_f8f6f4 v[36:39], v[128:135], v[162:169], v[226:229]
	v_mfma_f32_16x16x128_f8f6f4 v[28:31], v[136:143], v[162:169], v[230:233]
	v_mfma_f32_16x16x128_f8f6f4 v[20:23], v[128:135], v[170:177], v[234:237]
	v_mfma_f32_16x16x128_f8f6f4 v[12:15], v[136:143], v[170:177], v[238:241]
	v_mfma_f32_16x16x128_f8f6f4 v[4:7], v[128:135], v[178:185], v[242:245]
	v_mfma_f32_16x16x128_f8f6f4 v[0:3], v[136:143], v[178:185], v[246:249]
	s_setprio 0
	s_barrier
	s_add_i32 s79, s79, 2
	s_addk_i32 s80, 0x100
	s_cmp_gt_u32 s79, 13
	s_cbranch_scc1 .LBB0_2574
